# sel-phase block pairing: one proposal round instead of three (leftovers paired by rank); same math, different block order
# speedup vs baseline: 1.0121x; 1.0001x over previous
; template <bool DUMMY> __device__ __forceinline__ void sel_phase(Frame& F) {
;     ...
;             for (int r = 0; r < 3 && nB > 0; ++r) {
;                 if (F.tid < 128) PRP[F.tid] = 0xffffffffu;
;                 __syncthreads();
;                 const bool va = ia < npair && PB[ia] == (unsigned short)0xffffu; unsigned best = 0xffffffffu;
;                 if (va) { const unsigned pa = PW[ia]; const int klo = ia - 8 > 0 ? ia - 8 : 0, khi = ia + 8 < nB - 1 ? ia + 8 : nB - 1;
;                     for (int k = klo + sub; k <= khi; k += 4) if (MB[k] == 0) { const unsigned x = pa + PW[npair + k];
;                         const unsigned cst = (x != 0u) + (((x + 0x66666666u) & 0x88888888u) != 0u) + (((x + 0x55555555u) & 0x88888888u) != 0u) + (((x + 0x44444444u) & 0x88888888u) != 0u);
;                         const int dist = k > ia ? k - ia : ia - k;
;                         const unsigned key = (cst << 24) | ((unsigned)dist << 8) | (unsigned)k; best = key < best ? key : best; } }
;                 { const unsigned o1 = (unsigned)__builtin_amdgcn_mov_dpp((int)best, 0xB1, 0xF, 0xF, true); best = o1 < best ? o1 : best; const unsigned o2 = (unsigned)__builtin_amdgcn_mov_dpp((int)best, 0x4E, 0xF, 0xF, true); best = o2 < best ? o2 : best; }
;                 const bool prop = va && sub == 0 && best != 0xffffffffu; const unsigned kb_ = best & 0xffu, myp = ((best >> 24) << 16) | (unsigned)ia;
;                 if (prop) __hip_atomic_fetch_min(PRP + kb_, myp, __ATOMIC_RELAXED, __HIP_MEMORY_SCOPE_WORKGROUP);
;                 __syncthreads();
;                 if (prop && PRP[kb_] == myp) { PB[ia] = (unsigned short)(npair + kb_); MB[kb_] = 1; }
;                 __syncthreads();
;             }
.LBB0_1728:
	s_or_b64 exec, exec, s[64:65]
	s_add_i32 s45, s45, 1
	s_cmp_eq_u32 s45, 1
	s_waitcnt lgkmcnt(0)
	s_barrier
	s_cbranch_scc1 .LBB0_1746
